# prep_w1: prologue de-serialised (one 32-bit offset + scalar base/imm addressing, 12 VALU instead of ~45 before the loads)
# baseline (speedup 1.0000x reference)
_Z7prep_w1PKfPDv8_DF16_:
	s_load_dwordx4 s[4:7], s[0:1], 0x0
	s_lshl_b32 s0, s2, 8
	v_or_b32_e32 v4, s0, v0
	v_and_b32_e32 v5, 0xfffffc00, v4
	v_and_b32_e32 v6, 0x3c0, v4
	v_and_b32_e32 v7, 32, v4
	v_and_b32_e32 v8, 31, v4
	v_lshlrev_b32_e32 v5, 5, v5
	v_lshlrev_b32_e32 v6, 1, v6
	v_lshlrev_b32_e32 v7, 9, v7
	v_lshlrev_b32_e32 v8, 2, v8
	v_or3_b32 v5, v5, v6, v7
	v_or_b32_e32 v5, v5, v8
	v_add_u32_e32 v6, 0x1000, v5
	v_add_u32_e32 v7, 0x2000, v5
	v_add_u32_e32 v8, 0x3000, v5
	v_lshlrev_b32_e32 v4, 4, v4
	s_waitcnt lgkmcnt(0)
	global_load_dword v24, v5, s[4:5]
	global_load_dword v25, v5, s[4:5] offset:2048
	global_load_dword v20, v6, s[4:5]
	global_load_dword v21, v6, s[4:5] offset:2048
	global_load_dword v2, v7, s[4:5]
	global_load_dword v23, v7, s[4:5] offset:2048
	global_load_dword v3, v8, s[4:5]
	global_load_dword v22, v8, s[4:5] offset:2048
	s_waitcnt vmcnt(6)
	v_cvt_pk_f16_f32 v0, v24, v25
	s_waitcnt vmcnt(4)
	v_cvt_pk_f16_f32 v1, v20, v21
	s_waitcnt vmcnt(2)
	v_cvt_pk_f16_f32 v2, v2, v23
	s_waitcnt vmcnt(0)
	v_cvt_pk_f16_f32 v3, v3, v22
	global_store_dwordx4 v4, v[0:3], s[6:7]
	s_endpgm
